# attention: wave halves staggered by half a step (extra mid-step barrier) on top of pipelined conflict-free PV reads, mask skip and in-register reductions
# baseline (speedup 1.0000x reference)
; __device__ __forceinline__ void phase_attention(const Frame& F, const Args& a) {
;     ...
;     for (int unit = ((F.G % 8 == 0) ? (F.bid % 8) * (F.G / 8) + F.bid / 8 : F.bid); unit < 256; unit += F.G) {
;         const int b = unit >> 7, h = (unit >> 5) & 3, n = unit & 31;
;         const int kt_lo = (2 * n - 2) < 0 ? 0 : (2 * n - 2), kt_hi = (2 * n + 3) > 63 ? 63 : (2 * n + 3), nband = kt_hi - kt_lo + 1, ntile = nband + 4, nstep = 2 * ntile;
;         u32x4 kreg[2], vreg[2];
;         const bf16_t* kbase = QK + 2048 + h * 128 + 8 * c16; const bf16_t* vbase = VT + (size_t)(h * 128 + dim0) * T0 + 8 * c8;
;     ...
;         __syncthreads();
.LBB0_2770:
	v_readfirstlane_b32 s98, v0
	s_lshr_b32 s98, s98, 8
	s_cmp_lg_u32 s98, 0
	s_cbranch_scc1 .Latt_trail0
	s_barrier

; __device__ __forceinline__ void phase_attention(const Frame& F, const Args& a) {
;     ...
;         __syncthreads();
;         ATT_LOAD(0); ATT_STORE(0);
;         __syncthreads();
;         bf16x8 aq[2][4]; float mrun[2], lrun[2]; f32x4 o[2][8]; int qh = 0, qpos0 = 0, qrow = 0;
.LBB0_2776:
	s_bfe_u32 s10, s18, 0x20005
	s_lshl_b32 s1, s10, 7
	v_or_b32_e32 v3, s1, v174
	v_mul_u32_u24_e32 v66, 0x4400, v3
	s_lshl_b32 s6, s1, 1
	v_mov_b32_e32 v67, v2
	v_lshl_add_u64 v[162:163], v[152:153], 0, s[6:7]
	v_lshl_add_u64 v[164:165], v[156:157], 0, v[66:67]
	v_add_u32_e32 v3, s0, v173
	s_ashr_i32 s1, s0, 31
	v_mad_i64_i32 v[66:67], s[16:17], v3, s21, v[162:163]
	v_add_u32_e32 v3, 32, v3
	s_lshl_b64 s[0:1], s[0:1], 1
	v_lshl_add_u64 v[166:167], v[164:165], 0, s[8:9]
	v_mad_i64_i32 v[74:75], s[16:17], v3, s21, v[162:163]
	v_lshl_add_u64 v[78:79], v[164:165], 0, s[0:1]
	v_lshl_add_u64 v[82:83], v[166:167], 0, s[0:1]
	global_load_dwordx4 v[66:69], v[66:67], off
	s_nop 0
	global_load_dwordx4 v[74:77], v[74:75], off
	s_nop 0
	global_load_dwordx4 v[78:81], v[78:79], off
	s_nop 0
	global_load_dwordx4 v[82:85], v[82:83], off
	s_cmp_lt_i32 s27, -4
	s_waitcnt vmcnt(3)
	ds_write_b128 v178, v[66:69]
	s_waitcnt vmcnt(2)
	ds_write_b128 v178, v[74:77] offset:8704
	s_waitcnt vmcnt(1)
	v_add_u32_e32 v252, v179, v249
	v_add_u32_e32 v250, 0x4400, v252
	v_add_u32_e32 v251, 0x6800, v252
	ds_write2_b64 v250, v[78:79], v[80:81] offset1:2
	s_waitcnt vmcnt(0)
	ds_write2_b64 v251, v[82:83], v[84:85] offset1:2
	s_waitcnt lgkmcnt(0)
	s_barrier
	s_cbranch_scc1 .LBB0_2771
	v_readfirstlane_b32 s98, v0
	s_lshr_b32 s98, s98, 8
	s_cmp_eq_u32 s98, 0
	s_cbranch_scc1 .Latt_lead0
	s_barrier

; __device__ __forceinline__ void phase_attention(const Frame& F, const Args& a) {
;     ...
;                 float mx = s[m][0][0];
; #pragma unroll
;                 for (int nn = 0; nn < 4; ++nn)
; #pragma unroll
;                     for (int j = 0; j < 4; ++j) mx = fmaxf(mx, s[m][nn][j]);
;                 mx = fmaxf(mx, __shfl_xor(mx, 16)); mx = fmaxf(mx, __shfl_xor(mx, 32));
;                 const float mnew = fmaxf(mrun[m], mx), alpha = __expf(mrun[m] - mnew); mrun[m] = mnew;
;                 float rs = 0.f;
; #pragma unroll
;                 for (int nn = 0; nn < 4; ++nn)
; #pragma unroll
;                     for (int j = 0; j < 4; ++j) { const float p = __expf(s[m][nn][j] - mnew); s[m][nn][j] = p; rs += p; }
;                 rs += __shfl_xor(rs, 16); rs += __shfl_xor(rs, 32);
;                 lrun[m] = lrun[m] * alpha + rs;
; #pragma unroll
;                 for (int nd = 0; nd < 8; ++nd) o[m][nd] = o[m][nd] * alpha;
;     ...
;             if (step + 1 < nstep) ATT_STORE((step + 1) & 1);
.LBB0_2786:
	v_readfirstlane_b32 s98, v0
	s_lshr_b32 s98, s98, 8
	s_cmp_eq_u32 s98, 0
	s_cbranch_scc1 .Latt_mid0
	s_andn2_b64 vcc, exec, s[14:15]
	s_cbranch_vccnz .Latt_mid0
	s_bitcmp1_b32 s40, 0
	s_cselect_b32 s99, 0x8c00, 0
	v_add3_u32 v224, s99, v177, v150
	ds_write_b128 v224, v[66:69]
	ds_write_b128 v224, v[74:77] offset:8704
	v_add3_u32 v224, s99, v179, v249
	v_add_u32_e32 v225, 0x4400, v224
	v_add_u32_e32 v226, 0x6800, v224
	ds_write2_b64 v225, v[78:79], v[80:81] offset1:2
	ds_write2_b64 v226, v[82:83], v[84:85] offset1:2
.Latt_mid0:
	s_waitcnt lgkmcnt(0)
	s_barrier
	s_waitcnt lgkmcnt(0)
	v_add_f32_e32 v5, v142, v143
	v_max_f32_e32 v142, v139, v139
	v_max_f32_e32 v143, v138, v138
	v_max_f32_e32 v142, v143, v142
	v_max3_f32 v142, v142, v140, v141
	v_max3_f32 v142, v142, v134, v135
	v_max3_f32 v142, v142, v136, v137
	v_max3_f32 v142, v142, v130, v131
	v_max3_f32 v142, v142, v132, v133
	v_max3_f32 v142, v142, v122, v123
	v_max3_f32 v142, v142, v124, v125
	v_mov_b32_e32 v143, v142
	s_nop 1
	v_permlane16_swap_b32 v143, v142
	v_sub_f32_e32 v4, v4, v3
	v_mul_f32_e32 v4, 0x3fb8aa3b, v4
	v_exp_f32_e32 v4, v4
	s_add_i32 s0, s39, s42
	s_waitcnt lgkmcnt(0)
	v_max_f32_e32 v143, v143, v143
	v_max_f32_e32 v142, v142, v143
	v_mov_b32_e32 v143, v142
	s_nop 1
	v_permlane32_swap_b32 v143, v142
	v_fmac_f32_e32 v5, v189, v4
	v_pk_mul_f32 v[116:117], v[116:117], v[4:5] op_sel_hi:[1,0]
	v_pk_mul_f32 v[114:115], v[114:115], v[4:5] op_sel_hi:[1,0]
	v_pk_mul_f32 v[112:113], v[112:113], v[4:5] op_sel_hi:[1,0]
	s_waitcnt lgkmcnt(0)
	v_max3_f32 v142, v187, v142, v143
	v_sub_f32_e32 v138, v138, v142
	v_mul_f32_e32 v138, 0x3fb8aa3b, v138
	v_sub_f32_e32 v139, v139, v142
	v_exp_f32_e32 v138, v138
	v_mul_f32_e32 v139, 0x3fb8aa3b, v139
	v_sub_f32_e32 v140, v140, v142
	v_exp_f32_e32 v139, v139
	v_mul_f32_e32 v140, 0x3fb8aa3b, v140
	v_sub_f32_e32 v141, v141, v142
	v_exp_f32_e32 v140, v140
	v_mul_f32_e32 v141, 0x3fb8aa3b, v141
	v_sub_f32_e32 v134, v134, v142
	v_exp_f32_e32 v141, v141
	v_mul_f32_e32 v134, 0x3fb8aa3b, v134
	v_sub_f32_e32 v135, v135, v142
	v_add_f32_e32 v143, 0, v138
	v_exp_f32_e32 v134, v134
	v_mul_f32_e32 v135, 0x3fb8aa3b, v135
	v_sub_f32_e32 v136, v136, v142
	v_sub_f32_e32 v130, v130, v142
	v_add_f32_e32 v143, v139, v143
	v_exp_f32_e32 v135, v135
	v_mul_f32_e32 v136, 0x3fb8aa3b, v136
	v_sub_f32_e32 v137, v137, v142
	v_mul_f32_e32 v130, 0x3fb8aa3b, v130
	v_add_f32_e32 v143, v140, v143
	v_exp_f32_e32 v136, v136
	v_mul_f32_e32 v137, 0x3fb8aa3b, v137
	v_exp_f32_e32 v144, v130
	v_sub_f32_e32 v130, v131, v142
	v_add_f32_e32 v143, v141, v143
	v_exp_f32_e32 v137, v137
	v_mul_f32_e32 v130, 0x3fb8aa3b, v130
	v_add_f32_e32 v143, v134, v143
	v_exp_f32_e32 v145, v130
	v_sub_f32_e32 v130, v132, v142
	v_add_f32_e32 v143, v135, v143
	v_mul_f32_e32 v130, 0x3fb8aa3b, v130
	v_add_f32_e32 v143, v136, v143
	v_exp_f32_e32 v146, v130
	v_sub_f32_e32 v130, v133, v142
	v_sub_f32_e32 v122, v122, v142
	v_add_f32_e32 v143, v137, v143
	v_mul_f32_e32 v130, 0x3fb8aa3b, v130
	v_mul_f32_e32 v122, 0x3fb8aa3b, v122
	v_exp_f32_e32 v147, v130
	v_add_f32_e32 v130, v144, v143
	v_exp_f32_e32 v143, v122
	v_sub_f32_e32 v122, v123, v142
	v_mul_f32_e32 v122, 0x3fb8aa3b, v122
	v_exp_f32_e32 v123, v122
	v_sub_f32_e32 v122, v124, v142
	v_mul_f32_e32 v122, 0x3fb8aa3b, v122
	v_add_f32_e32 v130, v145, v130
	v_exp_f32_e32 v124, v122
	v_sub_f32_e32 v122, v125, v142
	v_add_f32_e32 v130, v146, v130
	v_mul_f32_e32 v122, 0x3fb8aa3b, v122
	v_add_f32_e32 v130, v147, v130
	v_exp_f32_e32 v125, v122
	v_add_f32_e32 v122, v143, v130
	v_add_f32_e32 v122, v123, v122
	v_add_f32_e32 v122, v124, v122
	v_add_f32_e32 v122, v125, v122
	v_mov_b32_e32 v130, v122
	s_nop 1
	v_permlane16_swap_b32 v130, v122
	v_pk_mul_f32 v[110:111], v[110:111], v[4:5] op_sel_hi:[1,0]
	v_pk_mul_f32 v[96:97], v[96:97], v[4:5] op_sel_hi:[1,0]
	v_pk_mul_f32 v[94:95], v[94:95], v[4:5] op_sel_hi:[1,0]
	v_pk_mul_f32 v[100:101], v[100:101], v[4:5] op_sel_hi:[1,0]
	s_waitcnt lgkmcnt(0)
	v_add_f32_e32 v122, v122, v130
	v_pk_mul_f32 v[98:99], v[98:99], v[4:5] op_sel_hi:[1,0]
	v_pk_mul_f32 v[104:105], v[104:105], v[4:5] op_sel_hi:[1,0]
	v_pk_mul_f32 v[102:103], v[102:103], v[4:5] op_sel_hi:[1,0]
	v_pk_mul_f32 v[108:109], v[108:109], v[4:5] op_sel_hi:[1,0]
	v_pk_mul_f32 v[106:107], v[106:107], v[4:5] op_sel_hi:[1,0]
	v_pk_mul_f32 v[88:89], v[88:89], v[4:5] op_sel_hi:[1,0]
	v_pk_mul_f32 v[86:87], v[86:87], v[4:5] op_sel_hi:[1,0]
	v_pk_mul_f32 v[92:93], v[92:93], v[4:5] op_sel_hi:[1,0]
	v_pk_mul_f32 v[90:91], v[90:91], v[4:5] op_sel_hi:[1,0]
	v_sub_f32_e32 v4, v187, v142
	v_mov_b32_e32 v130, v122
	s_nop 1
	v_permlane32_swap_b32 v130, v122
	v_mul_f32_e32 v4, 0x3fb8aa3b, v4
	v_exp_f32_e32 v4, v4
	s_add_i32 s0, s0, s43
	s_waitcnt lgkmcnt(0)
; #define LAS __attribute__((address_space(3)))
; __device__ __forceinline__ unsigned cvt_pk_bf16(float lo, float hi) { unsigned r; asm volatile("v_cvt_pk_bf16_f32 %0, %1, %2" : "=v"(r) : "v"(lo), "v"(hi)); return r; }
; __device__ __forceinline__ void phase_attention(const Frame& F, const Args& a) {
;     ...
;                 for (int ks = 0; ks < 2; ++ks) { u32x4 w; w.x = cvt_pk_bf16(s[m][2 * ks][0], s[m][2 * ks][1]); w.y = cvt_pk_bf16(s[m][2 * ks][2], s[m][2 * ks][3]);
;                     w.z = cvt_pk_bf16(s[m][2 * ks + 1][0], s[m][2 * ks + 1][1]); w.w = cvt_pk_bf16(s[m][2 * ks + 1][2], s[m][2 * ks + 1][3]); pf[m][ks] = __builtin_bit_cast(bf16x8, w); }
;             }
;             __builtin_amdgcn_s_setprio(1);
; #pragma unroll
;             for (int ks = 0; ks < 2; ++ks)
; #pragma unroll
;                 for (int nd = 0; nd < 8; ++nd) { const LAS bf16_t* vp = Vs + (16 * nd + fr) * 72 + 32 * ks + 4 * fq;
;                     u32x4 w; const u32x2 lo = *(const LAS u32x2*)vp, hi = *(const LAS u32x2*)(vp + 16); w.x = lo.x; w.y = lo.y; w.z = hi.x; w.w = hi.y;
;                     const bf16x8 vf = __builtin_bit_cast(bf16x8, w);
; #pragma unroll
;                     for (int m = 0; m < 2; ++m) o[m][nd] = __builtin_amdgcn_mfma_f32_16x16x32_bf16(vf, pf[m][ks], o[m][nd], 0, 0, 0); }
;     ...
;             if (step + 1 < nstep) ATT_STORE((step + 1) & 1);
	v_add_f32_e32 v122, v122, v130
	v_fmac_f32_e32 v122, v188, v4
	v_pk_mul_f32 v[72:73], v[72:73], v[4:5] op_sel_hi:[1,0]
	v_pk_mul_f32 v[70:71], v[70:71], v[4:5] op_sel_hi:[1,0]
	v_pk_mul_f32 v[64:65], v[64:65], v[4:5] op_sel_hi:[1,0]
	v_pk_mul_f32 v[62:63], v[62:63], v[4:5] op_sel_hi:[1,0]
	v_pk_mul_f32 v[60:61], v[60:61], v[4:5] op_sel_hi:[1,0]
	v_pk_mul_f32 v[58:59], v[58:59], v[4:5] op_sel_hi:[1,0]
	v_pk_mul_f32 v[56:57], v[56:57], v[4:5] op_sel_hi:[1,0]
	v_pk_mul_f32 v[54:55], v[54:55], v[4:5] op_sel_hi:[1,0]
	v_pk_mul_f32 v[52:53], v[52:53], v[4:5] op_sel_hi:[1,0]
	v_pk_mul_f32 v[50:51], v[50:51], v[4:5] op_sel_hi:[1,0]
	v_pk_mul_f32 v[48:49], v[48:49], v[4:5] op_sel_hi:[1,0]
	v_pk_mul_f32 v[46:47], v[46:47], v[4:5] op_sel_hi:[1,0]
	v_pk_mul_f32 v[44:45], v[44:45], v[4:5] op_sel_hi:[1,0]
	v_pk_mul_f32 v[42:43], v[42:43], v[4:5] op_sel_hi:[1,0]
	v_pk_mul_f32 v[40:41], v[40:41], v[4:5] op_sel_hi:[1,0]
	v_pk_mul_f32 v[38:39], v[38:39], v[4:5] op_sel_hi:[1,0]
	v_cvt_pk_bf16_f32 v130, v138, v139
	v_cvt_pk_bf16_f32 v131, v140, v141
	v_cvt_pk_bf16_f32 v132, v134, v135
	v_cvt_pk_bf16_f32 v133, v136, v137
	v_cvt_pk_bf16_f32 v134, v144, v145
	v_cvt_pk_bf16_f32 v135, v146, v147
	v_cvt_pk_bf16_f32 v136, v143, v123
	v_cvt_pk_bf16_f32 v137, v124, v125
	s_setprio 1
	v_add3_u32 v4, s44, v151, v176
	v_add_u32_e32 v123, 0x4000, v4
	v_add_u32_e32 v143, 0x4800, v4
	v_add_u32_e32 v144, 0x5000, v4
	v_add_u32_e32 v145, 0x5800, v4
	v_add_u32_e32 v146, 0x6800, v4
	v_add_u32_e32 v147, 0x7000, v4
	v_add_u32_e32 v148, 0x7800, v4
	v_add_u32_e32 v4, 0x8000, v4
	ds_read_b128 v[138:141], v123 offset:1024
	ds_read_b128 v[224:227], v143 offset:1280
	ds_read_b128 v[228:231], v144 offset:1536
	ds_read_b128 v[232:235], v145 offset:1792
	ds_read_b128 v[236:239], v146
	ds_read_b128 v[240:243], v147 offset:256
	ds_read_b128 v[244:247], v148 offset:512
	ds_read_b128 v[250:253], v4 offset:768
	s_waitcnt lgkmcnt(7)
	v_mfma_f32_16x16x32_bf16 v[114:117], v[138:141], v[126:129], v[114:117]
	v_mfma_f32_16x16x32_bf16 v[70:73], v[138:141], v[130:133], v[70:73]
	ds_read_b128 v[138:141], v123 offset:1088
	s_waitcnt lgkmcnt(7)
	v_mfma_f32_16x16x32_bf16 v[110:113], v[224:227], v[126:129], v[110:113]
	v_mfma_f32_16x16x32_bf16 v[62:65], v[224:227], v[130:133], v[62:65]
	ds_read_b128 v[224:227], v143 offset:1344
	s_waitcnt lgkmcnt(7)
	v_mfma_f32_16x16x32_bf16 v[94:97], v[228:231], v[126:129], v[94:97]
	v_mfma_f32_16x16x32_bf16 v[58:61], v[228:231], v[130:133], v[58:61]
	ds_read_b128 v[228:231], v144 offset:1600
	s_waitcnt lgkmcnt(7)
	v_mfma_f32_16x16x32_bf16 v[98:101], v[232:235], v[126:129], v[98:101]
	v_mfma_f32_16x16x32_bf16 v[54:57], v[232:235], v[130:133], v[54:57]
	ds_read_b128 v[232:235], v145 offset:1856
	s_waitcnt lgkmcnt(7)
	v_mfma_f32_16x16x32_bf16 v[102:105], v[236:239], v[126:129], v[102:105]
	v_mfma_f32_16x16x32_bf16 v[50:53], v[236:239], v[130:133], v[50:53]
	ds_read_b128 v[236:239], v146 offset:64
	s_waitcnt lgkmcnt(7)
	v_mfma_f32_16x16x32_bf16 v[106:109], v[240:243], v[126:129], v[106:109]
	v_mfma_f32_16x16x32_bf16 v[46:49], v[240:243], v[130:133], v[46:49]
	ds_read_b128 v[240:243], v147 offset:320
	s_waitcnt lgkmcnt(7)
	v_mfma_f32_16x16x32_bf16 v[86:89], v[244:247], v[126:129], v[86:89]
	v_mfma_f32_16x16x32_bf16 v[42:45], v[244:247], v[130:133], v[42:45]
	ds_read_b128 v[244:247], v148 offset:576
	s_waitcnt lgkmcnt(7)
	v_mfma_f32_16x16x32_bf16 v[90:93], v[250:253], v[126:129], v[90:93]
	v_mfma_f32_16x16x32_bf16 v[38:41], v[250:253], v[130:133], v[38:41]
	ds_read_b128 v[250:253], v4 offset:832
	s_waitcnt lgkmcnt(7)
	v_mfma_f32_16x16x32_bf16 v[114:117], v[138:141], v[118:121], v[114:117]
	v_mfma_f32_16x16x32_bf16 v[70:73], v[138:141], v[134:137], v[70:73]
	s_waitcnt lgkmcnt(6)
	v_mfma_f32_16x16x32_bf16 v[110:113], v[224:227], v[118:121], v[110:113]
	v_mfma_f32_16x16x32_bf16 v[62:65], v[224:227], v[134:137], v[62:65]
	s_waitcnt lgkmcnt(5)
	v_mfma_f32_16x16x32_bf16 v[94:97], v[228:231], v[118:121], v[94:97]
	v_mfma_f32_16x16x32_bf16 v[58:61], v[228:231], v[134:137], v[58:61]
	s_waitcnt lgkmcnt(4)
	v_mfma_f32_16x16x32_bf16 v[98:101], v[232:235], v[118:121], v[98:101]
	v_mfma_f32_16x16x32_bf16 v[54:57], v[232:235], v[134:137], v[54:57]
	s_waitcnt lgkmcnt(3)
	v_mfma_f32_16x16x32_bf16 v[102:105], v[236:239], v[118:121], v[102:105]
	v_mfma_f32_16x16x32_bf16 v[50:53], v[236:239], v[134:137], v[50:53]
	s_waitcnt lgkmcnt(2)
	v_mfma_f32_16x16x32_bf16 v[106:109], v[240:243], v[118:121], v[106:109]
	v_mfma_f32_16x16x32_bf16 v[46:49], v[240:243], v[134:137], v[46:49]
	s_waitcnt lgkmcnt(1)
	v_mfma_f32_16x16x32_bf16 v[86:89], v[244:247], v[118:121], v[86:89]
	v_mfma_f32_16x16x32_bf16 v[42:45], v[244:247], v[134:137], v[42:45]
	s_waitcnt lgkmcnt(0)
	v_mfma_f32_16x16x32_bf16 v[90:93], v[250:253], v[118:121], v[90:93]
	v_mfma_f32_16x16x32_bf16 v[38:41], v[250:253], v[134:137], v[38:41]
	s_setprio 0
	s_cmp_lg_u32 s0, 0
	s_cbranch_scc0 .LBB0_2791
	s_andn2_b64 vcc, exec, s[14:15]
	s_cbranch_vccnz .LBB0_2789
.LBB0_2788:
	v_readfirstlane_b32 s98, v0
	s_lshr_b32 s98, s98, 8
	s_cmp_lg_u32 s98, 0
	s_cbranch_scc1 .LBB0_2789
	s_bitcmp1_b32 s40, 0
	s_cselect_b32 s0, 0x8c00, 0
	s_add_i32 s0, s0, 0
	v_add3_u32 v4, s0, v177, v150
	ds_write_b128 v4, v[66:69]
	ds_write_b128 v4, v[74:77] offset:8704
	v_add3_u32 v4, s0, v179, v249
	v_add_u32_e32 v250, 0x4400, v4
	v_add_u32_e32 v251, 0x6800, v4
	ds_write2_b64 v250, v[78:79], v[80:81] offset1:2
	ds_write2_b64 v251, v[82:83], v[84:85] offset1:2
